# speedup vs baseline: 1.0055x; 1.0055x over previous
.LBB2_13:
	s_waitcnt vmcnt(0)
	s_barrier
	v_add_u32_e32 v34, s22, v109
	v_add_u32_e32 v34, 0xffff4000, v34
	v_and_b32_e32 v34, 0xc000, v34
	v_add_u32_e32 v114, 0, v34
	v_add_u32_e32 v38, v114, v106
	v_add_u32_e32 v82, v114, v105
	ds_read_b128 v[34:37], v38
	ds_read_b128 v[38:41], v38 offset:4096
	ds_read_b128 v[116:119], v82
	ds_read_b128 v[120:123], v82 offset:4096
	v_add_u32_e32 v82, v114, v104
	s_waitcnt lgkmcnt(2)
	v_mfma_f32_32x32x16_f16 v[50:65], v[34:37], v[78:81], 0
	v_mfma_f32_32x32x16_f16 v[34:49], v[38:41], v[78:81], 0
	s_waitcnt lgkmcnt(1)
	v_mfma_f32_32x32x16_f16 v[50:65], v[116:119], v[74:77], v[50:65]
	s_waitcnt lgkmcnt(0)
	v_mfma_f32_32x32x16_f16 v[34:49], v[120:123], v[74:77], v[34:49]
	ds_read_b128 v[116:119], v82
	ds_read_b128 v[120:123], v82 offset:4096
	v_add_u32_e32 v82, v114, v103
	s_waitcnt lgkmcnt(1)
	v_mfma_f32_32x32x16_f16 v[50:65], v[116:119], v[70:73], v[50:65]
	s_waitcnt lgkmcnt(0)
	v_mfma_f32_32x32x16_f16 v[34:49], v[120:123], v[70:73], v[34:49]
	ds_read_b128 v[116:119], v82
	ds_read_b128 v[120:123], v82 offset:4096
	s_waitcnt lgkmcnt(1)
	v_mfma_f32_32x32x16_f16 v[50:65], v[116:119], v[66:69], v[50:65]
	s_waitcnt lgkmcnt(0)
	v_mfma_f32_32x32x16_f16 v[34:49], v[120:123], v[66:69], v[34:49]
	s_add_i32 s16, s22, 0xffffc000
	s_and_b32 s16, s16, 0xc000
	v_add_u32_e32 v116, s16, v108
	s_add_u32 s16, s12, 0xfffce000
	s_addc_u32 s17, s13, -1
	v_readfirstlane_b32 s26, v116
	v_lshl_add_u64 v[116:117], s[16:17], 0, v[84:85]
	s_mov_b32 s27, m0
	s_mov_b32 m0, s26
	s_nop 0
	global_load_lds_dwordx4 v[116:117], off
	s_mov_b32 m0, s27
	v_lshl_add_u64 v[116:117], s[16:17], 0, v[86:87]
	s_add_i32 s16, s26, 0x400
	s_mov_b32 s17, m0
	s_mov_b32 m0, s16
	s_nop 0
	global_load_lds_dwordx4 v[116:117], off
	s_mov_b32 m0, s17
	s_and_b32 s16, s22, 0xc000
	v_add_u32_e32 v116, s16, v108
	s_nop 0
	v_readfirstlane_b32 s16, v116
	v_lshl_add_u64 v[116:117], s[12:13], 0, v[84:85]
	s_mov_b32 s17, m0
	s_mov_b32 m0, s16
	s_nop 0
	global_load_lds_dwordx4 v[116:117], off
	s_mov_b32 m0, s17
	v_lshl_add_u64 v[116:117], s[12:13], 0, v[86:87]
	s_addk_i32 s16, 0x400
	s_mov_b32 s17, m0
	s_mov_b32 m0, s16
	s_nop 0
	global_load_lds_dwordx4 v[116:117], off
	s_mov_b32 m0, s17
	v_max3_f32 v82, v50, v51, v52
	v_max3_f32 v82, v82, v53, v54
	v_max3_f32 v82, v82, v55, v56
	v_max3_f32 v82, v82, v57, v58
	v_max3_f32 v82, v82, v59, v60
	v_max3_f32 v82, v82, v61, v62
	v_max_f32_e32 v91, v65, v65
	v_max3_f32 v89, v34, v35, v36
	v_max3_f32 v89, v89, v37, v38
	v_max3_f32 v89, v89, v39, v40
	v_max3_f32 v89, v89, v41, v42
	v_max3_f32 v89, v89, v43, v44
	v_max3_f32 v89, v89, v45, v46
	v_max_f32_e32 v90, v49, v49
	v_max3_f32 v82, v82, v63, v64
	v_max3_f32 v89, v89, v47, v48
	v_max_f32_e32 v90, v91, v90
	v_max3_f32 v82, v82, v89, v90
	v_mov_b32_e32 v89, v82
	s_nop 1
	v_permlane32_swap_b32_e32 v82, v89
	v_max_f32_e32 v82, v82, v89
	v_fma_f32 v89, v82, s23, -v88
	v_cmp_lt_f32_e32 vcc, s24, v89
	s_cbranch_vccnz .Lattn_resc
	v_mov_b32_e32 v102, v88
.LBB2_12:
	v_cmp_neq_f32_e32 vcc, s25, v102
	v_add_u32_e32 v114, v114, v98
	v_add_u32_e32 v107, 2, v107
	v_cndmask_b32_e64 v124, v112, -v102, vcc
	v_fmamk_f32 v34, v34, 0x3e38aa3b, v124
	v_fmamk_f32 v50, v50, 0x3e38aa3b, v124
	v_exp_f32_e32 v126, v34
	v_fmamk_f32 v34, v51, 0x3e38aa3b, v124
	v_exp_f32_e32 v125, v50
	v_exp_f32_e32 v82, v34
	v_fmamk_f32 v34, v35, 0x3e38aa3b, v124
	v_exp_f32_e32 v34, v34
	v_add_f32_e32 v35, v126, v125
	v_fmamk_f32 v36, v36, 0x3e38aa3b, v124
	v_exp_f32_e32 v127, v36
	v_pk_add_f32 v[50:51], v[34:35], v[82:83]
	v_fmamk_f32 v35, v52, 0x3e38aa3b, v124
	v_pk_add_f32 v[88:89], v[50:51], v[50:51] op_sel_hi:[0,1]
	v_fmamk_f32 v36, v53, 0x3e38aa3b, v124
	v_exp_f32_e32 v35, v35
	v_exp_f32_e32 v88, v36
	v_fmamk_f32 v36, v37, 0x3e38aa3b, v124
	v_exp_f32_e32 v36, v36
	v_add_f32_e32 v37, v127, v35
	v_fmamk_f32 v38, v38, 0x3e38aa3b, v124
	v_exp_f32_e32 v115, v38
	v_pk_add_f32 v[50:51], v[36:37], v[88:89]
	v_fmamk_f32 v37, v54, 0x3e38aa3b, v124
	v_pk_add_f32 v[90:91], v[50:51], v[50:51] op_sel_hi:[0,1]
	v_fmamk_f32 v38, v55, 0x3e38aa3b, v124
	v_exp_f32_e32 v37, v37
	v_exp_f32_e32 v90, v38
	v_fmamk_f32 v38, v39, 0x3e38aa3b, v124
	v_exp_f32_e32 v50, v38
	v_add_f32_e32 v51, v115, v37
	s_add_u32 s12, s12, 0x64000
	s_addc_u32 s13, s13, 0
	v_pk_add_f32 v[38:39], v[50:51], v[90:91]
	s_add_i32 s22, s22, 0x8000
	v_pk_add_f32 v[54:55], v[38:39], v[38:39] op_sel_hi:[0,1]
	v_fmamk_f32 v38, v56, 0x3e38aa3b, v124
	v_exp_f32_e32 v51, v38
	v_fmamk_f32 v38, v40, 0x3e38aa3b, v124
	v_exp_f32_e32 v91, v38
	v_fmamk_f32 v38, v57, 0x3e38aa3b, v124
	v_exp_f32_e32 v54, v38
	v_fmamk_f32 v38, v41, 0x3e38aa3b, v124
	v_exp_f32_e32 v52, v38
	v_add_f32_e32 v53, v91, v51
	v_cvt_pk_f16_f32 v57, v51, v54
	v_cvt_pk_f16_f32 v56, v37, v90
	v_pk_add_f32 v[38:39], v[52:53], v[54:55]
	v_cvt_pk_f16_f32 v55, v35, v88
	v_pk_add_f32 v[116:117], v[38:39], v[38:39] op_sel_hi:[0,1]
	v_fmamk_f32 v38, v58, 0x3e38aa3b, v124
	v_exp_f32_e32 v53, v38
	v_fmamk_f32 v38, v42, 0x3e38aa3b, v124
	v_exp_f32_e32 v1, v38
	v_fmamk_f32 v38, v59, 0x3e38aa3b, v124
	v_exp_f32_e32 v116, v38
	v_fmamk_f32 v38, v43, 0x3e38aa3b, v124
	v_exp_f32_e32 v38, v38
	v_add_f32_e32 v39, v1, v53
	v_cvt_pk_f16_f32 v54, v125, v82
	v_fmamk_f32 v35, v64, 0x3e38aa3b, v124
	v_pk_add_f32 v[40:41], v[38:39], v[116:117]
	v_fmamk_f32 v39, v60, 0x3e38aa3b, v124
	v_pk_add_f32 v[118:119], v[40:41], v[40:41] op_sel_hi:[0,1]
	v_fmamk_f32 v40, v44, 0x3e38aa3b, v124
	v_exp_f32_e32 v117, v40
	v_fmamk_f32 v40, v61, 0x3e38aa3b, v124
	v_exp_f32_e32 v39, v39
	v_exp_f32_e32 v118, v40
	v_fmamk_f32 v40, v45, 0x3e38aa3b, v124
	v_exp_f32_e32 v40, v40
	v_add_f32_e32 v41, v117, v39
	v_exp_f32_e32 v82, v35
	v_fmamk_f32 v35, v65, 0x3e38aa3b, v124
	v_pk_add_f32 v[42:43], v[40:41], v[118:119]
	v_fmamk_f32 v41, v62, 0x3e38aa3b, v124
	v_pk_add_f32 v[120:121], v[42:43], v[42:43] op_sel_hi:[0,1]
	v_fmamk_f32 v42, v46, 0x3e38aa3b, v124
	v_exp_f32_e32 v119, v42
	v_fmamk_f32 v42, v63, 0x3e38aa3b, v124
	v_exp_f32_e32 v41, v41
	v_exp_f32_e32 v120, v42
	v_fmamk_f32 v42, v47, 0x3e38aa3b, v124
	v_exp_f32_e32 v122, v42
	ds_read_b64_tr_b16 v[42:43], v114 offset:8192
	ds_read_b64_tr_b16 v[44:45], v114 offset:8704
	v_add_f32_e32 v123, v119, v41
	ds_read_b64_tr_b16 v[58:59], v114 offset:9216
	ds_read_b64_tr_b16 v[60:61], v114 offset:9728
	v_pk_add_f32 v[46:47], v[122:123], v[120:121]
	s_waitcnt lgkmcnt(2)
	v_mfma_f32_32x32x16_f16 v[18:33], v[54:57], v[42:45], v[18:33]
	v_add_f32_e64 v88, v46, v46
	v_add_f32_e64 v89, v46, v47
	ds_read_b64_tr_b16 v[42:43], v114 offset:12288
	ds_read_b64_tr_b16 v[44:45], v114 offset:12800
	v_exp_f32_e32 v88, v35
	ds_read_b64_tr_b16 v[62:63], v114 offset:13312
	ds_read_b64_tr_b16 v[64:65], v114 offset:13824
	v_cvt_pk_f16_f32 v51, v127, v36
	v_cmp_le_u32_e32 vcc, s21, v107
	s_or_b64 s[14:15], vcc, s[14:15]
	s_waitcnt lgkmcnt(2)
	v_mfma_f32_32x32x16_f16 v[2:17], v[54:57], v[42:45], v[2:17]
	v_cvt_pk_f16_f32 v45, v82, v88
	v_cvt_pk_f16_f32 v44, v41, v120
	v_cvt_pk_f16_f32 v43, v39, v118
	v_cvt_pk_f16_f32 v42, v53, v116
	v_cvt_pk_f16_f32 v53, v91, v52
	v_cvt_pk_f16_f32 v52, v115, v50
	v_cvt_pk_f16_f32 v50, v126, v34
	v_mfma_f32_32x32x16_f16 v[18:33], v[42:45], v[58:61], v[18:33]
	v_fmamk_f32 v39, v48, 0x3e38aa3b, v124
	v_fmac_f32_e32 v124, 0x3e38aa3b, v49
	v_exp_f32_e32 v39, v39
	v_exp_f32_e32 v54, v124
	v_cvt_pk_f16_f32 v41, v117, v40
	v_cvt_pk_f16_f32 v40, v1, v38
	v_add_f32_e32 v55, v39, v82
	s_waitcnt lgkmcnt(0)
	v_mfma_f32_32x32x16_f16 v[2:17], v[42:45], v[62:65], v[2:17]
	ds_read_b64_tr_b16 v[42:43], v114 offset:10240
	ds_read_b64_tr_b16 v[44:45], v114 offset:10752
	ds_read_b64_tr_b16 v[34:35], v114 offset:11264
	ds_read_b64_tr_b16 v[36:37], v114 offset:11776
	s_waitcnt lgkmcnt(2)
	v_mfma_f32_32x32x16_f16 v[18:33], v[50:53], v[42:45], v[18:33]
	ds_read_b64_tr_b16 v[42:43], v114 offset:14336
	ds_read_b64_tr_b16 v[44:45], v114 offset:14848
	ds_read_b64_tr_b16 v[46:47], v114 offset:15360
	ds_read_b64_tr_b16 v[48:49], v114 offset:15872
	s_waitcnt lgkmcnt(2)
	v_mfma_f32_32x32x16_f16 v[2:17], v[50:53], v[42:45], v[2:17]
	v_cvt_pk_f16_f32 v43, v39, v54
	v_cvt_pk_f16_f32 v42, v119, v122
	s_nop 1
	v_mfma_f32_32x32x16_f16 v[18:33], v[40:43], v[34:37], v[18:33]
	v_add_f32_e64 v34, v54, v88
	v_add_f32_e64 v35, v55, v89
	v_mov_b32_e32 v88, v102
	v_add_f32_e32 v1, v34, v35
	v_add_f32_e32 v113, v113, v1
	s_waitcnt lgkmcnt(0)
	v_mfma_f32_32x32x16_f16 v[2:17], v[40:43], v[46:49], v[2:17]
	s_andn2_b64 exec, exec, s[14:15]
	s_cbranch_execnz .LBB2_13
	s_branch .LBB2_17
.Lattn_resc:
	v_mul_f32_e32 v82, 0x3e38aa3b, v82
	v_max_f32_e32 v82, v82, v82
	v_max_f32_e32 v89, v88, v88
	v_max_f32_e32 v102, v89, v82
	v_sub_f32_e32 v82, v88, v102
	v_exp_f32_e32 v82, v82
	s_and_saveexec_b64 s[16:17], s[4:5]
	s_cbranch_execz .LBB2_11
	v_lshl_add_u32 v88, v95, 2, v100
	ds_write_b32 v88, v82
	s_branch .LBB2_11
.LBB2_11:
	s_or_b64 exec, exec, s[16:17]
	s_waitcnt lgkmcnt(0)
	ds_read_b128 v[116:119], v111
	ds_read_b128 v[120:123], v111 offset:32
	ds_read_b128 v[124:127], v111 offset:64
	ds_read_b128 v[88:91], v111 offset:96
	v_mul_f32_e32 v113, v113, v82
	s_waitcnt lgkmcnt(3)
	v_pk_mul_f32 v[20:21], v[20:21], v[118:119]
	s_waitcnt lgkmcnt(2)
	v_pk_mul_f32 v[22:23], v[22:23], v[120:121]
	s_waitcnt lgkmcnt(1)
	v_pk_mul_f32 v[26:27], v[26:27], v[124:125]
	s_waitcnt lgkmcnt(0)
	v_pk_mul_f32 v[30:31], v[30:31], v[88:89]
	v_pk_mul_f32 v[32:33], v[32:33], v[90:91]
	v_pk_mul_f32 v[28:29], v[28:29], v[126:127]
	v_pk_mul_f32 v[24:25], v[24:25], v[122:123]
	v_pk_mul_f32 v[18:19], v[18:19], v[116:117]
	v_pk_mul_f32 v[14:15], v[14:15], v[88:89]
	v_pk_mul_f32 v[10:11], v[10:11], v[124:125]
	v_pk_mul_f32 v[6:7], v[6:7], v[120:121]
	v_pk_mul_f32 v[16:17], v[16:17], v[90:91]
	v_pk_mul_f32 v[12:13], v[12:13], v[126:127]
	v_pk_mul_f32 v[8:9], v[8:9], v[122:123]
	v_pk_mul_f32 v[4:5], v[4:5], v[118:119]
	v_pk_mul_f32 v[2:3], v[2:3], v[116:117]
	s_branch .LBB2_12
